# stream hand-rewrite M8: each wave keeps rows s,s+8,s+16,s+24 of a 32-row group in flight (16 loads), 104 VGPRs
# baseline (speedup 1.0000x reference)
_Z13stream_kernelPKfPf:
	s_load_dwordx4 s[4:7], s[0:1], 0x0
	s_movk_i32 s0, 0x100
	v_readfirstlane_b32 s3, v0
	v_cmp_gt_u32_e32 vcc, s0, v0
	s_and_saveexec_b64 s[0:1], vcc
	s_cbranch_execz .Lst_nou
	v_lshlrev_b32_e32 v18, 4, v0
	v_add_u32_e32 v19, 0x1000, v18
	v_add_u32_e32 v20, 0x2000, v18
	v_add_u32_e32 v21, 0x3000, v18
	s_waitcnt lgkmcnt(0)
	global_load_dwordx4 v[2:5], v18, s[6:7]
	global_load_dwordx4 v[6:9], v19, s[6:7]
	global_load_dwordx4 v[10:13], v20, s[6:7]
	global_load_dwordx4 v[14:17], v21, s[6:7]
	s_waitcnt vmcnt(2)
	v_pk_add_f32 v[4:5], v[4:5], v[8:9]
	v_pk_add_f32 v[2:3], v[2:3], v[6:7]
	s_waitcnt vmcnt(1)
	v_pk_add_f32 v[4:5], v[4:5], v[12:13]
	v_pk_add_f32 v[2:3], v[2:3], v[10:11]
	s_waitcnt vmcnt(0)
	v_pk_add_f32 v[4:5], v[4:5], v[16:17]
	v_pk_add_f32 v[2:3], v[2:3], v[14:15]
	s_nop 0
	ds_write_b128 v18, v[2:5]
.Lst_nou:
	s_or_b64 exec, exec, s[0:1]
	s_lshr_b32 s8, s3, 6
	v_and_b32_e32 v96, 63, v0
	v_lshlrev_b32_e32 v97, 4, v96
	s_lshr_b32 s10, s8, 3
	s_and_b32 s9, s8, 7
	s_lshl_b32 s11, s2, 7
	s_lshl_b32 s12, s10, 5
	s_lshl_b32 s24, s2, 5
	s_add_i32 s11, s11, s12
	s_add_i32 s11, s11, s9
	s_lshl_b32 s16, s11, 12
	s_add_i32 s17, s16, 0x8000
	s_add_i32 s18, s16, 0x10000
	s_add_i32 s19, s16, 0x18000
	s_add_i32 s20, s16, 0x40000
	s_add_i32 s21, s16, 0x48000
	s_add_i32 s22, s16, 0x50000
	s_add_i32 s23, s16, 0x58000
	s_waitcnt lgkmcnt(0)
	s_mov_b32 s0, s4
	s_and_b32 s1, s5, 0xffff
	s_brev_b32 s2, 16
	s_mov_b32 s3, 0x20000
	buffer_load_dwordx4 v[16:19], v97, s[0:3], s16 offen nt
	buffer_load_dwordx4 v[20:23], v97, s[0:3], s16 offen offset:1024 nt
	buffer_load_dwordx4 v[24:27], v97, s[0:3], s16 offen offset:2048 nt
	buffer_load_dwordx4 v[28:31], v97, s[0:3], s16 offen offset:3072 nt
	buffer_load_dwordx4 v[32:35], v97, s[0:3], s17 offen nt
	buffer_load_dwordx4 v[36:39], v97, s[0:3], s17 offen offset:1024 nt
	buffer_load_dwordx4 v[40:43], v97, s[0:3], s17 offen offset:2048 nt
	buffer_load_dwordx4 v[44:47], v97, s[0:3], s17 offen offset:3072 nt
	buffer_load_dwordx4 v[48:51], v97, s[0:3], s18 offen nt
	buffer_load_dwordx4 v[52:55], v97, s[0:3], s18 offen offset:1024 nt
	buffer_load_dwordx4 v[56:59], v97, s[0:3], s18 offen offset:2048 nt
	buffer_load_dwordx4 v[60:63], v97, s[0:3], s18 offen offset:3072 nt
	buffer_load_dwordx4 v[64:67], v97, s[0:3], s19 offen nt
	buffer_load_dwordx4 v[68:71], v97, s[0:3], s19 offen offset:1024 nt
	buffer_load_dwordx4 v[72:75], v97, s[0:3], s19 offen offset:2048 nt
	buffer_load_dwordx4 v[76:79], v97, s[0:3], s19 offen offset:3072 nt
	s_barrier
	ds_read_b128 v[0:3], v97
	ds_read_b128 v[4:7], v97 offset:1024
	ds_read_b128 v[8:11], v97 offset:2048
	ds_read_b128 v[12:15], v97 offset:3072
	v_mov_b32_e32 v95, 0
	s_waitcnt lgkmcnt(0)
	s_waitcnt vmcnt(12)
	v_pk_mul_f32 v[80:81], v[16:17], v[0:1]
	v_pk_mul_f32 v[82:83], v[18:19], v[2:3]
	v_pk_fma_f32 v[80:81], v[20:21], v[4:5], v[80:81]
	v_pk_fma_f32 v[82:83], v[22:23], v[6:7], v[82:83]
	v_pk_fma_f32 v[80:81], v[24:25], v[8:9], v[80:81]
	v_pk_fma_f32 v[82:83], v[26:27], v[10:11], v[82:83]
	v_pk_fma_f32 v[80:81], v[28:29], v[12:13], v[80:81]
	v_pk_fma_f32 v[82:83], v[30:31], v[14:15], v[82:83]
	buffer_load_dwordx4 v[16:19], v97, s[0:3], s20 offen nt
	buffer_load_dwordx4 v[20:23], v97, s[0:3], s20 offen offset:1024 nt
	buffer_load_dwordx4 v[24:27], v97, s[0:3], s20 offen offset:2048 nt
	buffer_load_dwordx4 v[28:31], v97, s[0:3], s20 offen offset:3072 nt
	v_pk_add_f32 v[80:81], v[80:81], v[82:83]
	v_cmp_eq_u32_e32 vcc, 0, v96
	v_add_f32_e32 v84, v80, v81
	s_nop 1
	v_add_f32_dpp v84, v84, v84 quad_perm:[1,0,3,2] row_mask:0xf bank_mask:0xf bound_ctrl:1
	s_nop 1
	v_add_f32_dpp v84, v84, v84 quad_perm:[2,3,0,1] row_mask:0xf bank_mask:0xf bound_ctrl:1
	s_nop 1
	v_add_f32_dpp v84, v84, v84 row_ror:4 row_mask:0xf bank_mask:0xf bound_ctrl:1
	s_nop 1
	v_add_f32_dpp v84, v84, v84 row_ror:8 row_mask:0xf bank_mask:0xf bound_ctrl:1
	v_mov_b32_e32 v85, v84
	s_nop 1
	v_permlane16_swap_b32_e32 v84, v85
	v_add_f32_e32 v84, v84, v85
	v_mov_b32_e32 v85, v84
	s_nop 1
	v_permlane32_swap_b32_e32 v84, v85
	v_add_f32_e32 v84, v84, v85
	v_cndmask_b32_e32 v95, v95, v84, vcc
	s_waitcnt vmcnt(12)
	v_pk_mul_f32 v[80:81], v[32:33], v[0:1]
	v_pk_mul_f32 v[82:83], v[34:35], v[2:3]
	v_pk_fma_f32 v[80:81], v[36:37], v[4:5], v[80:81]
	v_pk_fma_f32 v[82:83], v[38:39], v[6:7], v[82:83]
	v_pk_fma_f32 v[80:81], v[40:41], v[8:9], v[80:81]
	v_pk_fma_f32 v[82:83], v[42:43], v[10:11], v[82:83]
	v_pk_fma_f32 v[80:81], v[44:45], v[12:13], v[80:81]
	v_pk_fma_f32 v[82:83], v[46:47], v[14:15], v[82:83]
	buffer_load_dwordx4 v[32:35], v97, s[0:3], s21 offen nt
	buffer_load_dwordx4 v[36:39], v97, s[0:3], s21 offen offset:1024 nt
	buffer_load_dwordx4 v[40:43], v97, s[0:3], s21 offen offset:2048 nt
	buffer_load_dwordx4 v[44:47], v97, s[0:3], s21 offen offset:3072 nt
	v_pk_add_f32 v[80:81], v[80:81], v[82:83]
	v_cmp_eq_u32_e32 vcc, 1, v96
	v_add_f32_e32 v84, v80, v81
	s_nop 1
	v_add_f32_dpp v84, v84, v84 quad_perm:[1,0,3,2] row_mask:0xf bank_mask:0xf bound_ctrl:1
	s_nop 1
	v_add_f32_dpp v84, v84, v84 quad_perm:[2,3,0,1] row_mask:0xf bank_mask:0xf bound_ctrl:1
	s_nop 1
	v_add_f32_dpp v84, v84, v84 row_ror:4 row_mask:0xf bank_mask:0xf bound_ctrl:1
	s_nop 1
	v_add_f32_dpp v84, v84, v84 row_ror:8 row_mask:0xf bank_mask:0xf bound_ctrl:1
	v_mov_b32_e32 v85, v84
	s_nop 1
	v_permlane16_swap_b32_e32 v84, v85
	v_add_f32_e32 v84, v84, v85
	v_mov_b32_e32 v85, v84
	s_nop 1
	v_permlane32_swap_b32_e32 v84, v85
	v_add_f32_e32 v84, v84, v85
	v_cndmask_b32_e32 v95, v95, v84, vcc
	s_waitcnt vmcnt(12)
	v_pk_mul_f32 v[80:81], v[48:49], v[0:1]
	v_pk_mul_f32 v[82:83], v[50:51], v[2:3]
	v_pk_fma_f32 v[80:81], v[52:53], v[4:5], v[80:81]
	v_pk_fma_f32 v[82:83], v[54:55], v[6:7], v[82:83]
	v_pk_fma_f32 v[80:81], v[56:57], v[8:9], v[80:81]
	v_pk_fma_f32 v[82:83], v[58:59], v[10:11], v[82:83]
	v_pk_fma_f32 v[80:81], v[60:61], v[12:13], v[80:81]
	v_pk_fma_f32 v[82:83], v[62:63], v[14:15], v[82:83]
	buffer_load_dwordx4 v[48:51], v97, s[0:3], s22 offen nt
	buffer_load_dwordx4 v[52:55], v97, s[0:3], s22 offen offset:1024 nt
	buffer_load_dwordx4 v[56:59], v97, s[0:3], s22 offen offset:2048 nt
	buffer_load_dwordx4 v[60:63], v97, s[0:3], s22 offen offset:3072 nt
	v_pk_add_f32 v[80:81], v[80:81], v[82:83]
	v_cmp_eq_u32_e32 vcc, 2, v96
	v_add_f32_e32 v84, v80, v81
	s_nop 1
	v_add_f32_dpp v84, v84, v84 quad_perm:[1,0,3,2] row_mask:0xf bank_mask:0xf bound_ctrl:1
	s_nop 1
	v_add_f32_dpp v84, v84, v84 quad_perm:[2,3,0,1] row_mask:0xf bank_mask:0xf bound_ctrl:1
	s_nop 1
	v_add_f32_dpp v84, v84, v84 row_ror:4 row_mask:0xf bank_mask:0xf bound_ctrl:1
	s_nop 1
	v_add_f32_dpp v84, v84, v84 row_ror:8 row_mask:0xf bank_mask:0xf bound_ctrl:1
	v_mov_b32_e32 v85, v84
	s_nop 1
	v_permlane16_swap_b32_e32 v84, v85
	v_add_f32_e32 v84, v84, v85
	v_mov_b32_e32 v85, v84
	s_nop 1
	v_permlane32_swap_b32_e32 v84, v85
	v_add_f32_e32 v84, v84, v85
	v_cndmask_b32_e32 v95, v95, v84, vcc
	s_waitcnt vmcnt(12)
	v_pk_mul_f32 v[80:81], v[64:65], v[0:1]
	v_pk_mul_f32 v[82:83], v[66:67], v[2:3]
	v_pk_fma_f32 v[80:81], v[68:69], v[4:5], v[80:81]
	v_pk_fma_f32 v[82:83], v[70:71], v[6:7], v[82:83]
	v_pk_fma_f32 v[80:81], v[72:73], v[8:9], v[80:81]
	v_pk_fma_f32 v[82:83], v[74:75], v[10:11], v[82:83]
	v_pk_fma_f32 v[80:81], v[76:77], v[12:13], v[80:81]
	v_pk_fma_f32 v[82:83], v[78:79], v[14:15], v[82:83]
	buffer_load_dwordx4 v[64:67], v97, s[0:3], s23 offen nt
	buffer_load_dwordx4 v[68:71], v97, s[0:3], s23 offen offset:1024 nt
	buffer_load_dwordx4 v[72:75], v97, s[0:3], s23 offen offset:2048 nt
	buffer_load_dwordx4 v[76:79], v97, s[0:3], s23 offen offset:3072 nt
	v_pk_add_f32 v[80:81], v[80:81], v[82:83]
	v_cmp_eq_u32_e32 vcc, 3, v96
	v_add_f32_e32 v84, v80, v81
	s_nop 1
	v_add_f32_dpp v84, v84, v84 quad_perm:[1,0,3,2] row_mask:0xf bank_mask:0xf bound_ctrl:1
	s_nop 1
	v_add_f32_dpp v84, v84, v84 quad_perm:[2,3,0,1] row_mask:0xf bank_mask:0xf bound_ctrl:1
	s_nop 1
	v_add_f32_dpp v84, v84, v84 row_ror:4 row_mask:0xf bank_mask:0xf bound_ctrl:1
	s_nop 1
	v_add_f32_dpp v84, v84, v84 row_ror:8 row_mask:0xf bank_mask:0xf bound_ctrl:1
	v_mov_b32_e32 v85, v84
	s_nop 1
	v_permlane16_swap_b32_e32 v84, v85
	v_add_f32_e32 v84, v84, v85
	v_mov_b32_e32 v85, v84
	s_nop 1
	v_permlane32_swap_b32_e32 v84, v85
	v_add_f32_e32 v84, v84, v85
	v_cndmask_b32_e32 v95, v95, v84, vcc
	s_waitcnt vmcnt(12)
	v_pk_mul_f32 v[80:81], v[16:17], v[0:1]
	v_pk_mul_f32 v[82:83], v[18:19], v[2:3]
	v_pk_fma_f32 v[80:81], v[20:21], v[4:5], v[80:81]
	v_pk_fma_f32 v[82:83], v[22:23], v[6:7], v[82:83]
	v_pk_fma_f32 v[80:81], v[24:25], v[8:9], v[80:81]
	v_pk_fma_f32 v[82:83], v[26:27], v[10:11], v[82:83]
	v_pk_fma_f32 v[80:81], v[28:29], v[12:13], v[80:81]
	v_pk_fma_f32 v[82:83], v[30:31], v[14:15], v[82:83]
	s_nop 0
	v_pk_add_f32 v[80:81], v[80:81], v[82:83]
	v_cmp_eq_u32_e32 vcc, 4, v96
	v_add_f32_e32 v84, v80, v81
	s_nop 1
	v_add_f32_dpp v84, v84, v84 quad_perm:[1,0,3,2] row_mask:0xf bank_mask:0xf bound_ctrl:1
	s_nop 1
	v_add_f32_dpp v84, v84, v84 quad_perm:[2,3,0,1] row_mask:0xf bank_mask:0xf bound_ctrl:1
	s_nop 1
	v_add_f32_dpp v84, v84, v84 row_ror:4 row_mask:0xf bank_mask:0xf bound_ctrl:1
	s_nop 1
	v_add_f32_dpp v84, v84, v84 row_ror:8 row_mask:0xf bank_mask:0xf bound_ctrl:1
	v_mov_b32_e32 v85, v84
	s_nop 1
	v_permlane16_swap_b32_e32 v84, v85
	v_add_f32_e32 v84, v84, v85
	v_mov_b32_e32 v85, v84
	s_nop 1
	v_permlane32_swap_b32_e32 v84, v85
	v_add_f32_e32 v84, v84, v85
	v_cndmask_b32_e32 v95, v95, v84, vcc
	s_waitcnt vmcnt(8)
	v_pk_mul_f32 v[80:81], v[32:33], v[0:1]
	v_pk_mul_f32 v[82:83], v[34:35], v[2:3]
	v_pk_fma_f32 v[80:81], v[36:37], v[4:5], v[80:81]
	v_pk_fma_f32 v[82:83], v[38:39], v[6:7], v[82:83]
	v_pk_fma_f32 v[80:81], v[40:41], v[8:9], v[80:81]
	v_pk_fma_f32 v[82:83], v[42:43], v[10:11], v[82:83]
	v_pk_fma_f32 v[80:81], v[44:45], v[12:13], v[80:81]
	v_pk_fma_f32 v[82:83], v[46:47], v[14:15], v[82:83]
	s_nop 0
	v_pk_add_f32 v[80:81], v[80:81], v[82:83]
	v_cmp_eq_u32_e32 vcc, 5, v96
	v_add_f32_e32 v84, v80, v81
	s_nop 1
	v_add_f32_dpp v84, v84, v84 quad_perm:[1,0,3,2] row_mask:0xf bank_mask:0xf bound_ctrl:1
	s_nop 1
	v_add_f32_dpp v84, v84, v84 quad_perm:[2,3,0,1] row_mask:0xf bank_mask:0xf bound_ctrl:1
	s_nop 1
	v_add_f32_dpp v84, v84, v84 row_ror:4 row_mask:0xf bank_mask:0xf bound_ctrl:1
	s_nop 1
	v_add_f32_dpp v84, v84, v84 row_ror:8 row_mask:0xf bank_mask:0xf bound_ctrl:1
	v_mov_b32_e32 v85, v84
	s_nop 1
	v_permlane16_swap_b32_e32 v84, v85
	v_add_f32_e32 v84, v84, v85
	v_mov_b32_e32 v85, v84
	s_nop 1
	v_permlane32_swap_b32_e32 v84, v85
	v_add_f32_e32 v84, v84, v85
	v_cndmask_b32_e32 v95, v95, v84, vcc
	s_waitcnt vmcnt(4)
	v_pk_mul_f32 v[80:81], v[48:49], v[0:1]
	v_pk_mul_f32 v[82:83], v[50:51], v[2:3]
	v_pk_fma_f32 v[80:81], v[52:53], v[4:5], v[80:81]
	v_pk_fma_f32 v[82:83], v[54:55], v[6:7], v[82:83]
	v_pk_fma_f32 v[80:81], v[56:57], v[8:9], v[80:81]
	v_pk_fma_f32 v[82:83], v[58:59], v[10:11], v[82:83]
	v_pk_fma_f32 v[80:81], v[60:61], v[12:13], v[80:81]
	v_pk_fma_f32 v[82:83], v[62:63], v[14:15], v[82:83]
	s_nop 0
	v_pk_add_f32 v[80:81], v[80:81], v[82:83]
	v_cmp_eq_u32_e32 vcc, 6, v96
	v_add_f32_e32 v84, v80, v81
	s_nop 1
	v_add_f32_dpp v84, v84, v84 quad_perm:[1,0,3,2] row_mask:0xf bank_mask:0xf bound_ctrl:1
	s_nop 1
	v_add_f32_dpp v84, v84, v84 quad_perm:[2,3,0,1] row_mask:0xf bank_mask:0xf bound_ctrl:1
	s_nop 1
	v_add_f32_dpp v84, v84, v84 row_ror:4 row_mask:0xf bank_mask:0xf bound_ctrl:1
	s_nop 1
	v_add_f32_dpp v84, v84, v84 row_ror:8 row_mask:0xf bank_mask:0xf bound_ctrl:1
	v_mov_b32_e32 v85, v84
	s_nop 1
	v_permlane16_swap_b32_e32 v84, v85
	v_add_f32_e32 v84, v84, v85
	v_mov_b32_e32 v85, v84
	s_nop 1
	v_permlane32_swap_b32_e32 v84, v85
	v_add_f32_e32 v84, v84, v85
	v_cndmask_b32_e32 v95, v95, v84, vcc
	s_waitcnt vmcnt(0)
	v_pk_mul_f32 v[80:81], v[64:65], v[0:1]
	v_pk_mul_f32 v[82:83], v[66:67], v[2:3]
	v_pk_fma_f32 v[80:81], v[68:69], v[4:5], v[80:81]
	v_pk_fma_f32 v[82:83], v[70:71], v[6:7], v[82:83]
	v_pk_fma_f32 v[80:81], v[72:73], v[8:9], v[80:81]
	v_pk_fma_f32 v[82:83], v[74:75], v[10:11], v[82:83]
	v_pk_fma_f32 v[80:81], v[76:77], v[12:13], v[80:81]
	v_pk_fma_f32 v[82:83], v[78:79], v[14:15], v[82:83]
	s_nop 0
	v_pk_add_f32 v[80:81], v[80:81], v[82:83]
	v_cmp_eq_u32_e32 vcc, 7, v96
	v_add_f32_e32 v84, v80, v81
	s_nop 1
	v_add_f32_dpp v84, v84, v84 quad_perm:[1,0,3,2] row_mask:0xf bank_mask:0xf bound_ctrl:1
	s_nop 1
	v_add_f32_dpp v84, v84, v84 quad_perm:[2,3,0,1] row_mask:0xf bank_mask:0xf bound_ctrl:1
	s_nop 1
	v_add_f32_dpp v84, v84, v84 row_ror:4 row_mask:0xf bank_mask:0xf bound_ctrl:1
	s_nop 1
	v_add_f32_dpp v84, v84, v84 row_ror:8 row_mask:0xf bank_mask:0xf bound_ctrl:1
	v_mov_b32_e32 v85, v84
	s_nop 1
	v_permlane16_swap_b32_e32 v84, v85
	v_add_f32_e32 v84, v84, v85
	v_mov_b32_e32 v85, v84
	s_nop 1
	v_permlane32_swap_b32_e32 v84, v85
	v_add_f32_e32 v84, v84, v85
	v_cndmask_b32_e32 v95, v95, v84, vcc
	v_cmp_gt_u32_e32 vcc, 8, v96
	s_and_saveexec_b64 s[0:1], vcc
	v_and_b32_e32 v80, 1, v96
	v_lshlrev_b32_e32 v80, 16, v80
	v_and_b32_e32 v81, 2, v96
	v_lshl_or_b32 v80, v81, 1, v80
	v_and_b32_e32 v81, 4, v96
	v_lshl_or_b32 v80, v81, 2, v80
	s_lshl_b32 s9, s9, 13
	s_lshl_b32 s10, s10, 3
	s_add_i32 s9, s9, s24
	s_add_i32 s9, s9, s10
	s_addk_i32 s9, 0x6040
	v_add_u32_e32 v80, s9, v80
	global_store_dword v80, v95, s[6:7]
	s_endpgm

	.amdhsa_kernel _Z13stream_kernelPKfPf
		.amdhsa_group_segment_fixed_size 4096
		.amdhsa_private_segment_fixed_size 0
		.amdhsa_kernarg_size 16
		.amdhsa_user_sgpr_count 2
		.amdhsa_user_sgpr_dispatch_ptr 0
		.amdhsa_user_sgpr_queue_ptr 0
		.amdhsa_user_sgpr_kernarg_segment_ptr 1
		.amdhsa_user_sgpr_dispatch_id 0
		.amdhsa_user_sgpr_kernarg_preload_length 0
		.amdhsa_user_sgpr_kernarg_preload_offset 0
		.amdhsa_user_sgpr_private_segment_size 0
		.amdhsa_uses_dynamic_stack 0
		.amdhsa_enable_private_segment 0
		.amdhsa_system_sgpr_workgroup_id_x 1
		.amdhsa_system_sgpr_workgroup_id_y 0
		.amdhsa_system_sgpr_workgroup_id_z 0
		.amdhsa_system_sgpr_workgroup_info 0
		.amdhsa_system_vgpr_workitem_id 0
		.amdhsa_next_free_vgpr 98
		.amdhsa_next_free_sgpr 25
		.amdhsa_accum_offset 100
		.amdhsa_reserve_vcc 1
		.amdhsa_float_round_mode_32 0
		.amdhsa_float_round_mode_16_64 0
		.amdhsa_float_denorm_mode_32 3
		.amdhsa_float_denorm_mode_16_64 3
		.amdhsa_dx10_clamp 1
		.amdhsa_ieee_mode 1
		.amdhsa_fp16_overflow 0
		.amdhsa_tg_split 0
		.amdhsa_exception_fp_ieee_invalid_op 0
		.amdhsa_exception_fp_denorm_src 0
		.amdhsa_exception_fp_ieee_div_zero 0
		.amdhsa_exception_fp_ieee_overflow 0
		.amdhsa_exception_fp_ieee_underflow 0
		.amdhsa_exception_fp_ieee_inexact 0
		.amdhsa_exception_int_div_zero 0
	.end_amdhsa_kernel

.Lfunc_end1:
	.size	_Z13stream_kernelPKfPf, .Lfunc_end1-_Z13stream_kernelPKfPf
	.set _Z13stream_kernelPKfPf.num_vgpr, 98
	.set _Z13stream_kernelPKfPf.num_agpr, 0
	.set _Z13stream_kernelPKfPf.numbered_sgpr, 25
	.set _Z13stream_kernelPKfPf.num_named_barrier, 0
	.set _Z13stream_kernelPKfPf.private_seg_size, 0
	.set _Z13stream_kernelPKfPf.uses_vcc, 1
	.set _Z13stream_kernelPKfPf.uses_flat_scratch, 0
	.set _Z13stream_kernelPKfPf.has_dyn_sized_stack, 0
	.set _Z13stream_kernelPKfPf.has_recursion, 0
	.set _Z13stream_kernelPKfPf.has_indirect_call, 0

amdhsa.kernels:
  - .agpr_count:     0
    .args:
      - .actual_access:  read_only
        .address_space:  global
        .offset:         0
        .size:           8
        .value_kind:     global_buffer
      - .actual_access:  read_only
        .address_space:  global
        .offset:         8
        .size:           8
        .value_kind:     global_buffer
      - .actual_access:  read_only
        .address_space:  global
        .offset:         16
        .size:           8
        .value_kind:     global_buffer
      - .actual_access:  read_only
        .address_space:  global
        .offset:         24
        .size:           8
        .value_kind:     global_buffer
      - .actual_access:  write_only
        .address_space:  global
        .offset:         32
        .size:           8
        .value_kind:     global_buffer
    .group_segment_fixed_size: 2112
    .kernarg_segment_align: 8
    .kernarg_segment_size: 40
    .language:       OpenCL C
    .language_version:
      - 2
      - 0
    .max_flat_workgroup_size: 1024
    .name:           _Z11prep_kernelPKfS0_S0_S0_Pf
    .private_segment_fixed_size: 0
    .sgpr_count:     32
    .sgpr_spill_count: 0
    .symbol:         _Z11prep_kernelPKfS0_S0_S0_Pf.kd
    .uniform_work_group_size: 1
    .uses_dynamic_stack: false
    .vgpr_count:     40
    .vgpr_spill_count: 0
    .wavefront_size: 64
  - .agpr_count:     0
    .args:
      - .actual_access:  read_only
        .address_space:  global
        .offset:         0
        .size:           8
        .value_kind:     global_buffer
      - .address_space:  global
        .offset:         8
        .size:           8
        .value_kind:     global_buffer
    .group_segment_fixed_size: 4096
    .kernarg_segment_align: 8
    .kernarg_segment_size: 16
    .language:       OpenCL C
    .language_version:
      - 2
      - 0
    .max_flat_workgroup_size: 1024
    .name:           _Z13stream_kernelPKfPf
    .private_segment_fixed_size: 0
    .sgpr_count:     31
    .sgpr_spill_count: 0
    .symbol:         _Z13stream_kernelPKfPf.kd
    .uniform_work_group_size: 1
    .uses_dynamic_stack: false
    .vgpr_count:     98
    .vgpr_spill_count: 0
    .wavefront_size: 64
  - .agpr_count:     0
    .args:
      - .actual_access:  read_only
        .address_space:  global
        .offset:         0
        .size:           8
        .value_kind:     global_buffer
      - .actual_access:  write_only
        .address_space:  global
        .offset:         8
        .size:           8
        .value_kind:     global_buffer
    .group_segment_fixed_size: 32
    .kernarg_segment_align: 8
    .kernarg_segment_size: 16
    .language:       OpenCL C
    .language_version:
      - 2
      - 0
    .max_flat_workgroup_size: 256
    .name:           _Z14softmax_kernelPKfPf
    .private_segment_fixed_size: 0
    .sgpr_count:     16
    .sgpr_spill_count: 0
    .symbol:         _Z14softmax_kernelPKfPf.kd
    .uniform_work_group_size: 1
    .uses_dynamic_stack: false
    .vgpr_count:     17
    .vgpr_spill_count: 0
    .wavefront_size: 64
